# baseline (speedup 1.0000x reference)
.Lkv_poll:
	global_load_dword v227, v226, s[44:45] sc1
	s_waitcnt vmcnt(0)
	v_readfirstlane_b32 s46, v227
	s_cmp_ge_u32 s46, 0x100
	s_cbranch_scc1 .Lkv_nopoll
	s_add_i32 s47, s47, 1
	s_cmp_lt_u32 s47, 0x4000
	s_cbranch_scc0 .Lkv_nopoll
	s_sleep 16
	s_branch .Lkv_poll

.Ls2_spin2:
	global_load_dword v239, v238, s[54:55] offset:64 sc1
	s_waitcnt vmcnt(0)
	v_readfirstlane_b32 s59, v239
	s_cmp_ge_u32 s59, 0x100
	s_cbranch_scc1 .Ls2_plain
	s_add_i32 s58, s58, 1
	s_cmp_lt_u32 s58, 0x4000
	s_cbranch_scc0 .Ls2_plain
	s_sleep 4
	s_branch .Ls2_spin2

.Ls2_spin3:
	global_load_dword v239, v238, s[54:55] offset:128 sc1
	s_waitcnt vmcnt(0)
	v_readfirstlane_b32 s59, v239
	s_cmp_ge_u32 s59, 0x100
	s_cbranch_scc1 .Ls2_plain
	s_add_i32 s58, s58, 1
	s_cmp_lt_u32 s58, 0x4000
	s_cbranch_scc0 .Ls2_plain
	s_sleep 4
	s_branch .Ls2_spin3
